# indexer stored-score pass B: deferred pass-A stores behind K loads, overlapped LDS round trips and fewer VALU ops in the stored-score classification loop
# speedup vs baseline: 1.0329x; 1.0027x over previous
.LBB0_1297:
	v_readlane_b32 s14, v254, 48
	v_readlane_b32 s15, v254, 49
	s_andn2_b64 vcc, exec, s[14:15]
	s_cbranch_vccnz .LBB0_1558
	s_waitcnt lgkmcnt(0)
	s_add_u32 s22, s20, 0x2c200000
	s_addc_u32 s23, s21, 0
	s_add_u32 s18, s20, 0x3f700000
	s_addc_u32 s19, s21, 0
	s_add_u32 s24, s20, 0x2c400000
	s_addc_u32 s25, s21, 0
	s_add_u32 s26, s20, 0x2b200000
	v_readlane_b32 s14, v255, 0
	s_addc_u32 s27, s21, 0
	s_mov_b32 s76, s14
	s_lshl_b32 s100, s14, 19
	s_add_u32 s100, s100, 0x35d00000
	s_add_u32 s100, s20, s100
	s_addc_u32 s101, s21, 0
	v_mbcnt_lo_u32_b32 v230, -1, 0
	v_mbcnt_hi_u32_b32 v230, -1, v230
	v_lshlrev_b32_e32 v230, 4, v230
	v_readlane_b32 s15, v255, 1
	s_branch .LBB0_1300

.LBB0_1302:
	s_and_b64 s[14:15], s[28:29], exec
	s_cselect_b32 s14, s77, s76
	s_lshl_b32 s34, s14, 4
	s_mov_b32 s14, s33
	s_nop 0
	v_lshl_or_b32 v72, s14, 6, v195
	s_nop 0
	v_readfirstlane_b32 s14, v72
	s_ashr_i32 s30, s14, 6
	s_and_b32 s14, s34, 0xffffffc0
	s_add_i32 s14, s14, 64
	s_ashr_i32 s82, s14, 5
	v_and_b32_e32 v126, 63, v72
	v_and_b32_e32 v125, 15, v72
	s_cmpk_gt_i32 s14, 0x100
	s_mov_b64 s[14:15], -1
	s_cbranch_scc0 .LBB0_1545
	v_or_b32_e32 v0, s34, v125
	v_ashrrev_i32_e32 v1, 31, v0
	v_lshlrev_b64 v[2:3], 10, v[0:1]
	v_lshl_add_u64 v[2:3], s[26:27], 0, v[2:3]
	v_and_b32_e32 v176, 48, v126
	v_lshlrev_b64 v[0:1], 5, v[0:1]
	v_lshl_add_u64 v[68:69], v[2:3], 0, v[176:177]
	v_lshl_add_u64 v[12:13], s[24:25], 0, v[0:1]
	global_load_dwordx4 v[0:3], v[68:69], off
	global_load_dwordx4 v[4:7], v[68:69], off offset:64
	global_load_dwordx4 v[8:11], v[12:13], off offset:16
	s_nop 0
	global_load_dwordx4 v[12:15], v[12:13], off
	s_nop 0
	global_load_dwordx4 v[16:19], v[68:69], off offset:128
	global_load_dwordx4 v[20:23], v[68:69], off offset:192
	global_load_dwordx4 v[24:27], v[68:69], off offset:256
	global_load_dwordx4 v[28:31], v[68:69], off offset:320
	global_load_dwordx4 v[32:35], v[68:69], off offset:384
	global_load_dwordx4 v[36:39], v[68:69], off offset:448
	global_load_dwordx4 v[40:43], v[68:69], off offset:512
	global_load_dwordx4 v[44:47], v[68:69], off offset:576
	global_load_dwordx4 v[48:51], v[68:69], off offset:640
	global_load_dwordx4 v[52:55], v[68:69], off offset:704
	global_load_dwordx4 v[56:59], v[68:69], off offset:768
	global_load_dwordx4 v[60:63], v[68:69], off offset:832
	global_load_dwordx4 v[64:67], v[68:69], off offset:896
	s_nop 0
	global_load_dwordx4 v[68:71], v[68:69], off offset:960
	s_mov_b32 s74, s73
	s_mov_b32 s75, s73
	v_lshlrev_b32_e32 v73, 4, v72
	s_mov_b32 s72, s73
	v_mov_b64_e32 v[76:77], s[74:75]
	v_add_u32_e32 v122, 0, v73
	v_mov_b64_e32 v[74:75], s[72:73]
	v_cmp_gt_i32_e32 vcc, 17, v72
	s_waitcnt vmcnt(0)
	s_barrier
	ds_write_b128 v122, v[74:77]
	ds_write_b128 v122, v[74:77] offset:8192
	ds_write_b128 v122, v[74:77] offset:16384
	ds_write_b128 v122, v[74:77] offset:24576
	ds_write_b128 v122, v[74:77] offset:32768
	ds_write_b128 v122, v[74:77] offset:40960
	ds_write_b128 v122, v[74:77] offset:49152
	ds_write_b128 v122, v[74:77] offset:57344
	s_and_saveexec_b64 s[14:15], vcc
	v_lshl_add_u32 v72, v72, 2, s3
	ds_write_b32 v72, v177 offset:192
	s_or_b64 exec, exec, s[14:15]
	s_lshl_b32 s83, s30, 5
	v_or_b32_e32 v72, s83, v125
	v_lshrrev_b32_e32 v127, 4, v126
	v_ashrrev_i32_e32 v73, 31, v72
	v_lshlrev_b32_e32 v74, 3, v127
	v_mul_u32_u24_e32 v229, 0x70, v125
	v_lshlrev_b64 v[72:73], 7, v[72:73]
	v_sub_u32_e32 v72, v72, v229
	v_lshl_add_u64 v[72:73], s[22:23], 0, v[72:73]
	v_lshlrev_b32_e32 v176, 5, v74
	v_lshl_add_u64 v[72:73], v[72:73], 0, v[176:177]
	s_waitcnt lgkmcnt(0)
	s_barrier
	global_load_dwordx4 v[100:103], v[72:73], off
	global_load_dwordx4 v[96:99], v[72:73], off offset:1024
	global_load_dwordx4 v[92:95], v[72:73], off offset:2048
	global_load_dwordx4 v[88:91], v[72:73], off offset:3072
	s_cmp_lt_i32 s30, s82
	v_lshl_add_u32 v128, v125, 12, 0
	s_cselect_b64 s[36:37], -1, 0
	s_cmp_ge_i32 s30, s82
	v_lshl_add_u64 v[120:121], s[22:23], 0, v[176:177]
	s_cbranch_scc1 .LBB0_1310
	s_waitcnt vmcnt(0)
	v_mov_b64_e32 v[106:107], v[90:91]
	s_add_i32 s14, s82, -1
	s_mov_b32 s15, s30
	v_mov_b64_e32 v[104:105], v[88:89]
	v_mov_b32_e32 v116, v100
	v_mov_b32_e32 v117, v101
	v_mov_b32_e32 v118, v102
	v_mov_b32_e32 v119, v103
	v_mov_b32_e32 v108, v96
	v_mov_b32_e32 v109, v97
	v_mov_b32_e32 v110, v98
	v_mov_b32_e32 v111, v99
	v_mov_b32_e32 v112, v92
	v_mov_b32_e32 v113, v93
	v_mov_b32_e32 v114, v94
	v_mov_b32_e32 v115, v95
	v_add_u32_e32 v232, 0x7c000, v230
	s_branch .LBB0_1308

.LBB0_1308:
	s_waitcnt vmcnt(5)
	v_mfma_f32_16x16x32_bf16 v[130:133], v[116:119], v[0:3], 0
	s_min_i32 s32, s15, 0xf8
	v_lshl_add_u32 v231, s32, 11, v230
	s_add_i32 s31, s15, 8
	s_min_i32 s35, s31, s14
	v_lshl_or_b32 v72, s35, 5, v125
	s_waitcnt vmcnt(3)
	v_mfma_f32_16x16x32_bf16 v[134:137], v[112:115], v[0:3], 0
	v_ashrrev_i32_e32 v73, 31, v72
	v_lshlrev_b64 v[72:73], 7, v[72:73]
	v_sub_u32_e32 v72, v72, v229
	v_lshl_add_u64 v[84:85], v[120:121], 0, v[72:73]
	v_mfma_f32_16x16x32_bf16 v[138:141], v[108:111], v[4:7], v[130:133]
	global_load_dwordx4 v[72:75], v[84:85], off
	global_load_dwordx4 v[76:79], v[84:85], off offset:1024
	global_load_dwordx4 v[80:83], v[84:85], off offset:2048
	s_nop 0
	global_load_dwordx4 v[84:87], v[84:85], off offset:3072
	global_store_dwordx4 v232, v[156:159], s[100:101]
	global_store_dwordx4 v232, v[160:163], s[100:101] offset:1024
	s_nop 1
	v_mov_b32_e32 v156, 0
	s_add_i32 s15, s15, 16
	s_waitcnt vmcnt(8)
	v_mfma_f32_16x16x32_bf16 v[132:135], v[104:107], v[4:7], v[134:137]
	v_max_i32_e32 v123, 0, v138
	v_fmac_f32_e32 v156, v12, v123
	v_mov_b32_e32 v160, 0
	s_min_i32 s35, s15, s14
	s_cmp_ge_i32 s31, s82
	s_nop 3
	v_max_i32_e32 v124, 0, v132
	v_fmac_f32_e32 v160, v12, v124
	v_max_i32_e32 v124, 0, v139
	v_mov_b32_e32 v157, 0
	v_fmac_f32_e32 v157, v12, v124
	v_max_i32_e32 v129, 0, v133
	v_mov_b32_e32 v161, 0
	v_fmac_f32_e32 v161, v12, v129
	v_max_i32_e32 v129, 0, v140
	v_mov_b32_e32 v158, 0
	v_fmac_f32_e32 v158, v12, v129
	v_max_i32_e32 v130, 0, v134
	v_mov_b32_e32 v162, 0
	v_mfma_f32_16x16x32_bf16 v[136:139], v[116:119], v[16:19], 0
	v_fmac_f32_e32 v162, v12, v130
	v_max_i32_e32 v130, 0, v141
	v_mov_b32_e32 v159, 0
	v_mfma_f32_16x16x32_bf16 v[140:143], v[112:115], v[16:19], 0
	v_fmac_f32_e32 v159, v12, v130
	v_max_i32_e32 v135, 0, v135
	v_mov_b32_e32 v163, 0
	v_mfma_f32_16x16x32_bf16 v[136:139], v[108:111], v[20:23], v[136:139]
	v_fmac_f32_e32 v163, v12, v135
	v_mfma_f32_16x16x32_bf16 v[140:143], v[104:107], v[20:23], v[140:143]
	s_nop 6
	v_max_i32_e32 v135, 0, v136
	v_fmac_f32_e32 v156, v13, v135
	v_max_i32_e32 v135, 0, v140
	v_fmac_f32_e32 v160, v13, v135
	v_max_i32_e32 v135, 0, v137
	v_fmac_f32_e32 v157, v13, v135
	v_max_i32_e32 v135, 0, v141
	v_fmac_f32_e32 v161, v13, v135
	v_max_i32_e32 v135, 0, v138
	v_fmac_f32_e32 v158, v13, v135
	v_max_i32_e32 v135, 0, v142
	v_fmac_f32_e32 v162, v13, v135
	v_max_i32_e32 v135, 0, v139
	v_mfma_f32_16x16x32_bf16 v[136:139], v[116:119], v[24:27], 0
	v_fmac_f32_e32 v159, v13, v135
	v_max_i32_e32 v135, 0, v143
	v_fmac_f32_e32 v163, v13, v135
	v_mfma_f32_16x16x32_bf16 v[140:143], v[112:115], v[24:27], 0
	v_mfma_f32_16x16x32_bf16 v[136:139], v[108:111], v[28:31], v[136:139]
	v_mfma_f32_16x16x32_bf16 v[140:143], v[104:107], v[28:31], v[140:143]
	s_nop 6
	v_max_i32_e32 v135, 0, v136
	v_fmac_f32_e32 v156, v14, v135
	v_max_i32_e32 v135, 0, v140
	v_fmac_f32_e32 v160, v14, v135
	v_max_i32_e32 v135, 0, v137
	v_fmac_f32_e32 v157, v14, v135
	v_max_i32_e32 v135, 0, v141
	v_fmac_f32_e32 v161, v14, v135
	v_max_i32_e32 v135, 0, v138
	v_fmac_f32_e32 v158, v14, v135
	v_max_i32_e32 v135, 0, v142
	v_fmac_f32_e32 v162, v14, v135
	v_max_i32_e32 v135, 0, v139
	v_mfma_f32_16x16x32_bf16 v[136:139], v[116:119], v[32:35], 0
	v_fmac_f32_e32 v159, v14, v135
	v_max_i32_e32 v135, 0, v143
	v_fmac_f32_e32 v163, v14, v135
	v_mfma_f32_16x16x32_bf16 v[140:143], v[112:115], v[32:35], 0
	v_mfma_f32_16x16x32_bf16 v[136:139], v[108:111], v[36:39], v[136:139]
	v_mfma_f32_16x16x32_bf16 v[140:143], v[104:107], v[36:39], v[140:143]
	s_nop 6
	v_max_i32_e32 v135, 0, v136
	v_fmac_f32_e32 v156, v15, v135
	v_max_i32_e32 v135, 0, v140
	v_fmac_f32_e32 v160, v15, v135
	v_max_i32_e32 v135, 0, v137
	v_fmac_f32_e32 v157, v15, v135
	v_max_i32_e32 v135, 0, v141
	v_fmac_f32_e32 v161, v15, v135
	v_max_i32_e32 v135, 0, v138
	v_fmac_f32_e32 v158, v15, v135
	v_max_i32_e32 v135, 0, v142
	v_fmac_f32_e32 v162, v15, v135
	v_max_i32_e32 v135, 0, v139
	v_mfma_f32_16x16x32_bf16 v[136:139], v[116:119], v[40:43], 0
	v_fmac_f32_e32 v159, v15, v135
	v_max_i32_e32 v135, 0, v143
	v_fmac_f32_e32 v163, v15, v135
	v_mfma_f32_16x16x32_bf16 v[140:143], v[112:115], v[40:43], 0
	v_mfma_f32_16x16x32_bf16 v[136:139], v[108:111], v[44:47], v[136:139]
	v_mfma_f32_16x16x32_bf16 v[140:143], v[104:107], v[44:47], v[140:143]
	s_nop 6
	v_max_i32_e32 v135, 0, v136
	v_fmac_f32_e32 v156, v8, v135
	v_max_i32_e32 v135, 0, v140
	v_fmac_f32_e32 v160, v8, v135
	v_max_i32_e32 v135, 0, v137
	v_fmac_f32_e32 v157, v8, v135
	v_max_i32_e32 v135, 0, v141
	v_fmac_f32_e32 v161, v8, v135
	v_max_i32_e32 v135, 0, v138
	v_fmac_f32_e32 v158, v8, v135
	v_max_i32_e32 v135, 0, v142
	v_fmac_f32_e32 v162, v8, v135
	v_max_i32_e32 v135, 0, v139
	v_mfma_f32_16x16x32_bf16 v[136:139], v[116:119], v[48:51], 0
	v_fmac_f32_e32 v159, v8, v135
	v_max_i32_e32 v135, 0, v143
	v_fmac_f32_e32 v163, v8, v135
	v_mfma_f32_16x16x32_bf16 v[140:143], v[112:115], v[48:51], 0
	v_mfma_f32_16x16x32_bf16 v[136:139], v[108:111], v[52:55], v[136:139]
	v_mfma_f32_16x16x32_bf16 v[140:143], v[104:107], v[52:55], v[140:143]
	s_nop 6
	v_max_i32_e32 v135, 0, v136
	v_fmac_f32_e32 v156, v9, v135
	v_max_i32_e32 v135, 0, v140
	v_fmac_f32_e32 v160, v9, v135
	v_max_i32_e32 v135, 0, v137
	v_fmac_f32_e32 v157, v9, v135
	v_max_i32_e32 v135, 0, v141
	v_fmac_f32_e32 v161, v9, v135
	v_max_i32_e32 v135, 0, v138
	v_fmac_f32_e32 v158, v9, v135
	v_max_i32_e32 v135, 0, v142
	v_fmac_f32_e32 v162, v9, v135
	v_max_i32_e32 v135, 0, v139
	v_mfma_f32_16x16x32_bf16 v[136:139], v[116:119], v[56:59], 0
	v_fmac_f32_e32 v159, v9, v135
	v_max_i32_e32 v135, 0, v143
	v_fmac_f32_e32 v163, v9, v135
	v_mfma_f32_16x16x32_bf16 v[140:143], v[112:115], v[56:59], 0
	v_mfma_f32_16x16x32_bf16 v[112:115], v[112:115], v[64:67], 0
	v_mfma_f32_16x16x32_bf16 v[116:119], v[116:119], v[64:67], 0
	v_mfma_f32_16x16x32_bf16 v[136:139], v[108:111], v[60:63], v[136:139]
	v_mfma_f32_16x16x32_bf16 v[140:143], v[104:107], v[60:63], v[140:143]
	v_mfma_f32_16x16x32_bf16 v[104:107], v[104:107], v[68:71], v[112:115]
	s_nop 5
	v_max_i32_e32 v135, 0, v136
	v_fmac_f32_e32 v156, v10, v135
	v_max_i32_e32 v135, 0, v140
	v_mfma_f32_16x16x32_bf16 v[108:111], v[108:111], v[68:71], v[116:119]
	v_fmac_f32_e32 v160, v10, v135
	v_max_i32_e32 v104, 0, v104
	v_max_i32_e32 v135, 0, v137
	v_fmac_f32_e32 v157, v10, v135
	v_fmac_f32_e32 v160, v11, v104
	s_nop 5
	v_max_i32_e32 v104, 0, v109
	v_max_i32_e32 v135, 0, v141
	v_fmac_f32_e32 v161, v10, v135
	v_fmac_f32_e32 v157, v11, v104
	v_max_i32_e32 v104, 0, v105
	v_max_i32_e32 v135, 0, v138
	v_fmac_f32_e32 v158, v10, v135
	v_fmac_f32_e32 v161, v11, v104
	v_max_i32_e32 v104, 0, v110
	v_max_i32_e32 v135, 0, v142
	v_fmac_f32_e32 v162, v10, v135
	v_fmac_f32_e32 v158, v11, v104
	v_max_i32_e32 v104, 0, v106
	v_max_i32_e32 v135, 0, v139
	v_fmac_f32_e32 v159, v10, v135
	v_fmac_f32_e32 v162, v11, v104
	v_max_i32_e32 v104, 0, v111
	v_max_i32_e32 v135, 0, v143
	v_fmac_f32_e32 v163, v10, v135
	v_fmac_f32_e32 v159, v11, v104
	v_max_i32_e32 v104, 0, v107
	v_max_i32_e32 v108, 0, v108
	v_fmac_f32_e32 v156, v11, v108
	v_fmac_f32_e32 v163, v11, v104
	s_nop 0
	v_lshrrev_b32 v104, 22, v156
	v_bfe_u32 v105, v156, 21, 1
	v_lshl_add_u32 v104, v104, 2, v128
	v_mad_u32_u24 v105, v105, s1, 1
	ds_add_u32 v104, v105
	v_lshrrev_b32 v104, 22, v157
	v_bfe_u32 v105, v157, 21, 1
	v_lshl_add_u32 v104, v104, 2, v128
	v_mad_u32_u24 v105, v105, s1, 1
	ds_add_u32 v104, v105
	v_lshrrev_b32 v104, 22, v158
	v_bfe_u32 v105, v158, 21, 1
	v_lshl_add_u32 v104, v104, 2, v128
	v_mad_u32_u24 v105, v105, s1, 1
	ds_add_u32 v104, v105
	v_lshrrev_b32 v104, 22, v159
	v_bfe_u32 v105, v159, 21, 1
	v_lshl_add_u32 v104, v104, 2, v128
	v_mad_u32_u24 v105, v105, s1, 1
	ds_add_u32 v104, v105
	v_lshrrev_b32 v104, 22, v160
	v_bfe_u32 v105, v160, 21, 1
	v_lshl_add_u32 v104, v104, 2, v128
	v_mad_u32_u24 v105, v105, s1, 1
	ds_add_u32 v104, v105
	v_lshrrev_b32 v104, 22, v161
	v_bfe_u32 v105, v161, 21, 1
	v_lshl_add_u32 v104, v104, 2, v128
	v_mad_u32_u24 v105, v105, s1, 1
	ds_add_u32 v104, v105
	v_lshrrev_b32 v104, 22, v162
	v_bfe_u32 v105, v162, 21, 1
	v_lshl_add_u32 v104, v104, 2, v128
	v_mad_u32_u24 v105, v105, s1, 1
	ds_add_u32 v104, v105
	v_lshrrev_b32 v104, 22, v163
	v_bfe_u32 v105, v163, 21, 1
	v_lshl_add_u32 v104, v104, 2, v128
	v_mad_u32_u24 v105, v105, s1, 1
	ds_add_u32 v104, v105
	v_lshl_or_b32 v104, s35, 5, v125
	v_ashrrev_i32_e32 v105, 31, v104
	v_lshlrev_b64 v[104:105], 7, v[104:105]
	v_sub_u32_e32 v104, v104, v229
	v_lshl_add_u64 v[104:105], v[120:121], 0, v[104:105]
	global_load_dwordx4 v[116:119], v[104:105], off
	global_load_dwordx4 v[108:111], v[104:105], off offset:1024
	global_load_dwordx4 v[112:115], v[104:105], off offset:2048
	s_nop 0
	global_load_dwordx4 v[104:107], v[104:105], off offset:3072
	global_store_dwordx4 v231, v[156:159], s[100:101]
	global_store_dwordx4 v231, v[160:163], s[100:101] offset:1024
	s_cbranch_scc1 .LBB0_1307
	s_waitcnt vmcnt(11)
	v_mfma_f32_16x16x32_bf16 v[130:133], v[72:75], v[0:3], 0
	s_min_i32 s32, s31, 0xf8
	v_lshl_add_u32 v232, s32, 11, v230
	s_waitcnt vmcnt(9)
	v_mfma_f32_16x16x32_bf16 v[134:137], v[80:83], v[0:3], 0
	v_mfma_f32_16x16x32_bf16 v[138:141], v[76:79], v[4:7], v[130:133]
	s_waitcnt vmcnt(8)
	v_mfma_f32_16x16x32_bf16 v[132:135], v[84:87], v[4:7], v[134:137]
	s_nop 2
	v_mov_b32_e32 v156, 0
	s_nop 1
	v_max_i32_e32 v123, 0, v138
	v_fmac_f32_e32 v156, v12, v123
	v_mov_b32_e32 v160, 0
	v_max_i32_e32 v124, 0, v132
	v_fmac_f32_e32 v160, v12, v124
	v_max_i32_e32 v124, 0, v139
	v_mov_b32_e32 v157, 0
	v_fmac_f32_e32 v157, v12, v124
	v_max_i32_e32 v129, 0, v133
	v_mov_b32_e32 v161, 0
	v_fmac_f32_e32 v161, v12, v129
	v_max_i32_e32 v129, 0, v140
	v_mov_b32_e32 v158, 0
	v_fmac_f32_e32 v158, v12, v129
	v_max_i32_e32 v130, 0, v134
	v_mov_b32_e32 v162, 0
	v_mfma_f32_16x16x32_bf16 v[136:139], v[72:75], v[16:19], 0
	v_fmac_f32_e32 v162, v12, v130
	v_max_i32_e32 v130, 0, v141
	v_mov_b32_e32 v159, 0
	v_mfma_f32_16x16x32_bf16 v[140:143], v[80:83], v[16:19], 0
	v_fmac_f32_e32 v159, v12, v130
	v_max_i32_e32 v135, 0, v135
	v_mov_b32_e32 v163, 0
	v_mfma_f32_16x16x32_bf16 v[136:139], v[76:79], v[20:23], v[136:139]
	v_fmac_f32_e32 v163, v12, v135
	v_mfma_f32_16x16x32_bf16 v[140:143], v[84:87], v[20:23], v[140:143]
	s_nop 6
	v_max_i32_e32 v135, 0, v136
	v_fmac_f32_e32 v156, v13, v135
	v_max_i32_e32 v135, 0, v140
	v_fmac_f32_e32 v160, v13, v135
	v_max_i32_e32 v135, 0, v137
	v_fmac_f32_e32 v157, v13, v135
	v_max_i32_e32 v135, 0, v141
	v_fmac_f32_e32 v161, v13, v135
	v_max_i32_e32 v135, 0, v138
	v_fmac_f32_e32 v158, v13, v135
	v_max_i32_e32 v135, 0, v142
	v_fmac_f32_e32 v162, v13, v135
	v_max_i32_e32 v135, 0, v139
	v_mfma_f32_16x16x32_bf16 v[136:139], v[72:75], v[24:27], 0
	v_fmac_f32_e32 v159, v13, v135
	v_max_i32_e32 v135, 0, v143
	v_fmac_f32_e32 v163, v13, v135
	v_mfma_f32_16x16x32_bf16 v[140:143], v[80:83], v[24:27], 0
	v_mfma_f32_16x16x32_bf16 v[136:139], v[76:79], v[28:31], v[136:139]
	v_mfma_f32_16x16x32_bf16 v[140:143], v[84:87], v[28:31], v[140:143]
	s_nop 6
	v_max_i32_e32 v135, 0, v136
	v_fmac_f32_e32 v156, v14, v135
	v_max_i32_e32 v135, 0, v140
	v_fmac_f32_e32 v160, v14, v135
	v_max_i32_e32 v135, 0, v137
	v_fmac_f32_e32 v157, v14, v135
	v_max_i32_e32 v135, 0, v141
	v_fmac_f32_e32 v161, v14, v135
	v_max_i32_e32 v135, 0, v138
	v_fmac_f32_e32 v158, v14, v135
	v_max_i32_e32 v135, 0, v142
	v_fmac_f32_e32 v162, v14, v135
	v_max_i32_e32 v135, 0, v139
	v_mfma_f32_16x16x32_bf16 v[136:139], v[72:75], v[32:35], 0
	v_fmac_f32_e32 v159, v14, v135
	v_max_i32_e32 v135, 0, v143
	v_fmac_f32_e32 v163, v14, v135
	v_mfma_f32_16x16x32_bf16 v[140:143], v[80:83], v[32:35], 0
	v_mfma_f32_16x16x32_bf16 v[136:139], v[76:79], v[36:39], v[136:139]
	v_mfma_f32_16x16x32_bf16 v[140:143], v[84:87], v[36:39], v[140:143]
	s_nop 6
	v_max_i32_e32 v135, 0, v136
	v_fmac_f32_e32 v156, v15, v135
	v_max_i32_e32 v135, 0, v140
	v_fmac_f32_e32 v160, v15, v135
	v_max_i32_e32 v135, 0, v137
	v_fmac_f32_e32 v157, v15, v135
	v_max_i32_e32 v135, 0, v141
	v_fmac_f32_e32 v161, v15, v135
	v_max_i32_e32 v135, 0, v138
	v_fmac_f32_e32 v158, v15, v135
	v_max_i32_e32 v135, 0, v142
	v_fmac_f32_e32 v162, v15, v135
	v_max_i32_e32 v135, 0, v139
	v_mfma_f32_16x16x32_bf16 v[136:139], v[72:75], v[40:43], 0
	v_fmac_f32_e32 v159, v15, v135
	v_max_i32_e32 v135, 0, v143
	v_fmac_f32_e32 v163, v15, v135
	v_mfma_f32_16x16x32_bf16 v[140:143], v[80:83], v[40:43], 0
	v_mfma_f32_16x16x32_bf16 v[136:139], v[76:79], v[44:47], v[136:139]
	v_mfma_f32_16x16x32_bf16 v[140:143], v[84:87], v[44:47], v[140:143]
	s_nop 6
	v_max_i32_e32 v135, 0, v136
	v_fmac_f32_e32 v156, v8, v135
	v_max_i32_e32 v135, 0, v140
	v_fmac_f32_e32 v160, v8, v135
	v_max_i32_e32 v135, 0, v137
	v_fmac_f32_e32 v157, v8, v135
	v_max_i32_e32 v135, 0, v141
	v_fmac_f32_e32 v161, v8, v135
	v_max_i32_e32 v135, 0, v138
	v_fmac_f32_e32 v158, v8, v135
	v_max_i32_e32 v135, 0, v142
	v_fmac_f32_e32 v162, v8, v135
	v_max_i32_e32 v135, 0, v139
	v_mfma_f32_16x16x32_bf16 v[136:139], v[72:75], v[48:51], 0
	v_fmac_f32_e32 v159, v8, v135
	v_max_i32_e32 v135, 0, v143
	v_fmac_f32_e32 v163, v8, v135
	v_mfma_f32_16x16x32_bf16 v[140:143], v[80:83], v[48:51], 0
	v_mfma_f32_16x16x32_bf16 v[136:139], v[76:79], v[52:55], v[136:139]
	v_mfma_f32_16x16x32_bf16 v[140:143], v[84:87], v[52:55], v[140:143]
	s_nop 6
	v_max_i32_e32 v135, 0, v136
	v_fmac_f32_e32 v156, v9, v135
	v_max_i32_e32 v135, 0, v140
	v_fmac_f32_e32 v160, v9, v135
	v_max_i32_e32 v135, 0, v137
	v_fmac_f32_e32 v157, v9, v135
	v_max_i32_e32 v135, 0, v141
	v_fmac_f32_e32 v161, v9, v135
	v_max_i32_e32 v135, 0, v138
	v_fmac_f32_e32 v158, v9, v135
	v_max_i32_e32 v135, 0, v142
	v_fmac_f32_e32 v162, v9, v135
	v_max_i32_e32 v135, 0, v139
	v_mfma_f32_16x16x32_bf16 v[136:139], v[72:75], v[56:59], 0
	v_fmac_f32_e32 v159, v9, v135
	v_max_i32_e32 v135, 0, v143
	v_fmac_f32_e32 v163, v9, v135
	v_mfma_f32_16x16x32_bf16 v[140:143], v[80:83], v[56:59], 0
	v_mfma_f32_16x16x32_bf16 v[136:139], v[76:79], v[60:63], v[136:139]
	v_mfma_f32_16x16x32_bf16 v[140:143], v[84:87], v[60:63], v[140:143]
	s_nop 6
	v_max_i32_e32 v135, 0, v136
	v_fmac_f32_e32 v156, v10, v135
	v_max_i32_e32 v135, 0, v140
	v_fmac_f32_e32 v160, v10, v135
	v_max_i32_e32 v135, 0, v137
	v_fmac_f32_e32 v157, v10, v135
	v_max_i32_e32 v135, 0, v141
	v_fmac_f32_e32 v161, v10, v135
	v_max_i32_e32 v135, 0, v138
	v_fmac_f32_e32 v158, v10, v135
	v_max_i32_e32 v135, 0, v142
	v_fmac_f32_e32 v162, v10, v135
	v_max_i32_e32 v135, 0, v139
	v_mfma_f32_16x16x32_bf16 v[136:139], v[72:75], v[64:67], 0
	v_fmac_f32_e32 v159, v10, v135
	v_max_i32_e32 v135, 0, v143
	v_fmac_f32_e32 v163, v10, v135
	v_mfma_f32_16x16x32_bf16 v[140:143], v[80:83], v[64:67], 0
	v_mfma_f32_16x16x32_bf16 v[136:139], v[76:79], v[68:71], v[136:139]
	v_mfma_f32_16x16x32_bf16 v[140:143], v[84:87], v[68:71], v[140:143]
	s_nop 6
	v_max_i32_e32 v135, 0, v136
	v_fmac_f32_e32 v156, v11, v135
	v_max_i32_e32 v135, 0, v140
	v_fmac_f32_e32 v160, v11, v135
	v_max_i32_e32 v135, 0, v137
	v_fmac_f32_e32 v157, v11, v135
	v_max_i32_e32 v135, 0, v141
	v_fmac_f32_e32 v161, v11, v135
	v_max_i32_e32 v135, 0, v138
	v_fmac_f32_e32 v158, v11, v135
	v_max_i32_e32 v135, 0, v142
	v_fmac_f32_e32 v162, v11, v135
	v_max_i32_e32 v135, 0, v139
	v_fmac_f32_e32 v159, v11, v135
	v_max_i32_e32 v135, 0, v143
	v_fmac_f32_e32 v163, v11, v135
	v_lshrrev_b32 v135, 22, v156
	v_bfe_u32 v131, v156, 21, 1
	v_mad_u32_u24 v131, v131, s1, 1
	v_lshl_add_u32 v135, v135, 2, v128
	ds_add_u32 v135, v131
	v_lshrrev_b32 v131, 22, v157
	v_bfe_u32 v132, v157, 21, 1
	v_lshl_add_u32 v131, v131, 2, v128
	v_mad_u32_u24 v132, v132, s1, 1
	ds_add_u32 v131, v132
	v_lshrrev_b32 v131, 22, v158
	v_bfe_u32 v132, v158, 21, 1
	v_lshl_add_u32 v131, v131, 2, v128
	v_mad_u32_u24 v132, v132, s1, 1
	ds_add_u32 v131, v132
	v_lshrrev_b32 v131, 22, v159
	v_bfe_u32 v132, v159, 21, 1
	v_lshl_add_u32 v131, v131, 2, v128
	v_mad_u32_u24 v132, v132, s1, 1
	ds_add_u32 v131, v132
	v_lshrrev_b32 v131, 22, v160
	v_bfe_u32 v123, v160, 21, 1
	v_mad_u32_u24 v123, v123, s1, 1
	v_lshl_add_u32 v131, v131, 2, v128
	ds_add_u32 v131, v123
	v_lshrrev_b32 v123, 22, v161
	v_bfe_u32 v124, v161, 21, 1
	v_lshl_add_u32 v123, v123, 2, v128
	v_mad_u32_u24 v124, v124, s1, 1
	ds_add_u32 v123, v124
	v_lshrrev_b32 v123, 22, v162
	v_bfe_u32 v124, v162, 21, 1
	v_lshl_add_u32 v123, v123, 2, v128
	v_mad_u32_u24 v124, v124, s1, 1
	ds_add_u32 v123, v124
	v_lshrrev_b32 v123, 22, v163
	v_bfe_u32 v124, v163, 21, 1
	v_lshl_add_u32 v123, v123, 2, v128
	v_mad_u32_u24 v124, v124, s1, 1
	ds_add_u32 v123, v124
	s_cmp_ge_i32 s15, s82
	s_cbranch_scc0 .LBB0_1308
	global_store_dwordx4 v232, v[156:159], s[100:101]
	global_store_dwordx4 v232, v[160:163], s[100:101] offset:1024
	s_branch .LBB0_1310

.Lpb2_entry:
	s_waitcnt vmcnt(0)
	s_min_i32 s32, s82, 0xf8
	v_mov_b32_e32 v235, 0xffff
	v_ashrrev_i32_e32 v244, 31, v139
	v_lshl_add_u32 v233, s31, 11, v230
	global_load_dwordx4 v[156:159], v233, s[100:101]
	global_load_dwordx4 v[160:163], v233, s[100:101] offset:1024
	v_mov_b32_e32 v234, 0x7c000
	global_store_dword v234, v193, s[100:101]
	s_add_i32 s85, s31, 8
	v_lshl_add_u32 v233, s85, 11, v230
	global_load_dwordx4 v[178:181], v233, s[100:101]
	global_load_dwordx4 v[182:185], v233, s[100:101] offset:1024
	global_store_dword v234, v193, s[100:101]
.Lpb2_i0:
	s_add_i32 s85, s31, 16
	s_min_i32 s85, s85, 0xff
	v_lshl_add_u32 v233, s85, 11, v230
	global_load_dwordx4 v[236:239], v233, s[100:101]
	global_load_dwordx4 v[240:243], v233, s[100:101] offset:1024
	s_waitcnt vmcnt(6)
	v_cmp_ge_f32_e64 s[66:67], v156, v140
	v_cmp_ge_f32_e64 s[50:51], v156, v139
	v_cmp_ge_f32_e32 vcc, v157, v140
	v_cmp_ge_f32_e64 s[52:53], v157, v139
	v_cndmask_b32_e64 v224, 0, 1, s[66:67]
	v_cndmask_b32_e64 v225, 0, 2, vcc
	s_andn2_b64 s[50:51], s[50:51], s[66:67]
	s_andn2_b64 s[52:53], s[52:53], vcc
	v_or_b32_e32 v228, v224, v225
	v_cmp_ge_f32_e64 s[66:67], v158, v140
	v_cmp_ge_f32_e64 s[54:55], v158, v139
	v_cmp_ge_f32_e32 vcc, v159, v140
	v_cmp_ge_f32_e64 s[56:57], v159, v139
	v_cndmask_b32_e64 v224, 0, 4, s[66:67]
	v_cndmask_b32_e64 v225, 0, 8, vcc
	s_andn2_b64 s[54:55], s[54:55], s[66:67]
	s_andn2_b64 s[56:57], s[56:57], vcc
	v_or3_b32 v228, v228, v224, v225
	v_cmp_ge_f32_e64 s[66:67], v160, v140
	v_cmp_ge_f32_e64 s[58:59], v160, v139
	v_cmp_ge_f32_e32 vcc, v161, v140
	v_cmp_ge_f32_e64 s[60:61], v161, v139
	v_cndmask_b32_e64 v224, 0, v201, s[66:67]
	v_cndmask_b32_e64 v225, 0, v200, vcc
	s_andn2_b64 s[58:59], s[58:59], s[66:67]
	s_andn2_b64 s[60:61], s[60:61], vcc
	v_or3_b32 v228, v228, v224, v225
	v_cmp_ge_f32_e64 s[66:67], v162, v140
	v_cmp_ge_f32_e64 s[62:63], v162, v139
	v_cmp_ge_f32_e32 vcc, v163, v140
	v_cmp_ge_f32_e64 s[64:65], v163, v139
	v_cndmask_b32_e64 v224, 0, v199, s[66:67]
	v_cndmask_b32_e64 v225, 0, v198, vcc
	s_andn2_b64 s[62:63], s[62:63], s[66:67]
	s_andn2_b64 s[64:65], s[64:65], vcc
	v_or3_b32 v228, v228, v224, v225
	v_lshlrev_b32_e32 v104, v143, v228
	ds_bpermute_b32 v105, v144, v104
	v_mov_b32_e32 v227, s96
	s_mov_b64 s[14:15], exec
	s_mov_b64 exec, s[50:51]
	ds_add_rtn_u32 v214, v142, v193
	s_mov_b64 exec, s[52:53]
	ds_add_rtn_u32 v215, v142, v193
	s_mov_b64 exec, s[54:55]
	ds_add_rtn_u32 v216, v142, v193
	s_mov_b64 exec, s[56:57]
	ds_add_rtn_u32 v217, v142, v193
	s_mov_b64 exec, s[58:59]
	ds_add_rtn_u32 v218, v142, v193
	s_mov_b64 exec, s[60:61]
	ds_add_rtn_u32 v219, v142, v193
	s_mov_b64 exec, s[62:63]
	ds_add_rtn_u32 v220, v142, v193
	s_mov_b64 exec, s[64:65]
	ds_add_rtn_u32 v221, v142, v193
	s_mov_b64 exec, s[50:51]
	v_xor_b32_e32 v206, v244, v156
	v_bfe_u32 v222, v206, 11, 10
	v_bfe_u32 v223, v206, 10, 1
	v_lshl_add_u32 v222, v222, 2, v128
	v_mad_u32_u24 v223, v223, v235, 1
	ds_add_u32 v222, v223
	s_mov_b64 exec, s[52:53]
	v_xor_b32_e32 v207, v244, v157
	v_bfe_u32 v222, v207, 11, 10
	v_bfe_u32 v223, v207, 10, 1
	v_lshl_add_u32 v222, v222, 2, v128
	v_mad_u32_u24 v223, v223, v235, 1
	ds_add_u32 v222, v223
	s_mov_b64 exec, s[54:55]
	v_xor_b32_e32 v208, v244, v158
	v_bfe_u32 v222, v208, 11, 10
	v_bfe_u32 v223, v208, 10, 1
	v_lshl_add_u32 v222, v222, 2, v128
	v_mad_u32_u24 v223, v223, v235, 1
	ds_add_u32 v222, v223
	s_mov_b64 exec, s[56:57]
	v_xor_b32_e32 v209, v244, v159
	v_bfe_u32 v222, v209, 11, 10
	v_bfe_u32 v223, v209, 10, 1
	v_lshl_add_u32 v222, v222, 2, v128
	v_mad_u32_u24 v223, v223, v235, 1
	ds_add_u32 v222, v223
	s_waitcnt lgkmcnt(8)
	s_mov_b64 exec, s[58:59]
	v_xor_b32_e32 v210, v244, v160
	v_bfe_u32 v222, v210, 11, 10
	v_bfe_u32 v223, v210, 10, 1
	v_lshl_add_u32 v222, v222, 2, v128
	v_mad_u32_u24 v223, v223, v235, 1
	ds_add_u32 v222, v223
	s_mov_b64 exec, s[60:61]
	v_xor_b32_e32 v211, v244, v161
	v_bfe_u32 v222, v211, 11, 10
	v_bfe_u32 v223, v211, 10, 1
	v_lshl_add_u32 v222, v222, 2, v128
	v_mad_u32_u24 v223, v223, v235, 1
	ds_add_u32 v222, v223
	s_mov_b64 exec, s[62:63]
	v_xor_b32_e32 v212, v244, v162
	v_bfe_u32 v222, v212, 11, 10
	v_bfe_u32 v223, v212, 10, 1
	v_lshl_add_u32 v222, v222, 2, v128
	v_mad_u32_u24 v223, v223, v235, 1
	ds_add_u32 v222, v223
	s_mov_b64 exec, s[64:65]
	v_xor_b32_e32 v213, v244, v163
	v_bfe_u32 v222, v213, 11, 10
	v_bfe_u32 v223, v213, 10, 1
	v_lshl_add_u32 v222, v222, 2, v128
	v_mad_u32_u24 v223, v223, v235, 1
	ds_add_u32 v222, v223
	s_waitcnt lgkmcnt(8)
	s_mov_b64 exec, s[14:15]
	v_or_b32_e32 v104, v105, v104
	ds_bpermute_b32 v105, v145, v104
	s_mov_b64 exec, s[50:51]
	v_cmp_lt_u32_e64 s[66:67], s0, v214
	s_add_i32 s85, s74, 0x0
	v_bfe_u32 v224, v206, 10, 11
	v_lshl_add_u32 v222, v214, 2, v141
	v_add3_u32 v224, v224, v124, s85
	s_andn2_b64 exec, exec, s[66:67]
	ds_write_b32 v222, v224
	s_mov_b64 exec, s[66:67]
	ds_write_b32 v227, v193
	s_mov_b64 exec, s[52:53]
	v_cmp_lt_u32_e64 s[66:67], s0, v215
	s_add_i32 s85, s74, 0x800
	v_bfe_u32 v224, v207, 10, 11
	v_lshl_add_u32 v222, v215, 2, v141
	v_add3_u32 v224, v224, v124, s85
	s_andn2_b64 exec, exec, s[66:67]
	ds_write_b32 v222, v224
	s_mov_b64 exec, s[66:67]
	ds_write_b32 v227, v193
	s_waitcnt lgkmcnt(8)
	s_mov_b64 exec, s[54:55]
	v_cmp_lt_u32_e64 s[66:67], s0, v216
	s_add_i32 s85, s74, 0x1000
	v_bfe_u32 v224, v208, 10, 11
	v_lshl_add_u32 v222, v216, 2, v141
	v_add3_u32 v224, v224, v124, s85
	s_andn2_b64 exec, exec, s[66:67]
	ds_write_b32 v222, v224
	s_mov_b64 exec, s[66:67]
	ds_write_b32 v227, v193
	s_mov_b64 exec, s[56:57]
	v_cmp_lt_u32_e64 s[66:67], s0, v217
	s_add_i32 s85, s74, 0x1800
	v_bfe_u32 v224, v209, 10, 11
	v_lshl_add_u32 v222, v217, 2, v141
	v_add3_u32 v224, v224, v124, s85
	s_andn2_b64 exec, exec, s[66:67]
	ds_write_b32 v222, v224
	s_mov_b64 exec, s[66:67]
	ds_write_b32 v227, v193
	s_waitcnt lgkmcnt(8)
	s_mov_b64 exec, s[58:59]
	v_cmp_lt_u32_e64 s[66:67], s0, v218
	s_add_i32 s85, s74, 0x8000
	v_bfe_u32 v224, v210, 10, 11
	v_lshl_add_u32 v222, v218, 2, v141
	v_add3_u32 v224, v224, v124, s85
	s_andn2_b64 exec, exec, s[66:67]
	ds_write_b32 v222, v224
	s_mov_b64 exec, s[66:67]
	ds_write_b32 v227, v193
	s_mov_b64 exec, s[60:61]
	v_cmp_lt_u32_e64 s[66:67], s0, v219
	s_add_i32 s85, s74, 0x8800
	v_bfe_u32 v224, v211, 10, 11
	v_lshl_add_u32 v222, v219, 2, v141
	v_add3_u32 v224, v224, v124, s85
	s_andn2_b64 exec, exec, s[66:67]
	ds_write_b32 v222, v224
	s_mov_b64 exec, s[66:67]
	ds_write_b32 v227, v193
	s_waitcnt lgkmcnt(8)
	s_mov_b64 exec, s[62:63]
	v_cmp_lt_u32_e64 s[66:67], s0, v220
	s_add_i32 s85, s74, 0x9000
	v_bfe_u32 v224, v212, 10, 11
	v_lshl_add_u32 v222, v220, 2, v141
	v_add3_u32 v224, v224, v124, s85
	s_andn2_b64 exec, exec, s[66:67]
	ds_write_b32 v222, v224
	s_mov_b64 exec, s[66:67]
	ds_write_b32 v227, v193
	s_mov_b64 exec, s[64:65]
	v_cmp_lt_u32_e64 s[66:67], s0, v221
	s_add_i32 s85, s74, 0x9800
	v_bfe_u32 v224, v213, 10, 11
	v_lshl_add_u32 v222, v221, 2, v141
	v_add3_u32 v224, v224, v124, s85
	s_andn2_b64 exec, exec, s[66:67]
	ds_write_b32 v222, v224
	s_mov_b64 exec, s[66:67]
	ds_write_b32 v227, v193
	s_mov_b64 exec, s[14:15]
	s_and_saveexec_b64 s[14:15], s[38:39]
	v_or_b32_e32 v106, v104, v105
	v_lshl_add_u64 v[104:105], v[122:123], 0, s[74:75]
	v_add_co_u32_e32 v104, vcc, 0x3f700000, v104
	s_nop 1
	v_addc_co_u32_e32 v105, vcc, 0, v105, vcc
	global_store_dword v[104:105], v106, off
	s_or_b64 exec, exec, s[14:15]
	s_add_u32 s74, s74, 0x80000
	s_addc_u32 s75, s75, 0
	s_add_i32 s31, s31, 8
	s_cmp_ge_i32 s31, s32
	s_cbranch_scc1 .Lpb2_done
.Lpb2_i1:
	s_add_i32 s85, s31, 16
	s_min_i32 s85, s85, 0xff
	v_lshl_add_u32 v233, s85, 11, v230
	global_load_dwordx4 v[156:159], v233, s[100:101]
	global_load_dwordx4 v[160:163], v233, s[100:101] offset:1024
	s_waitcnt vmcnt(6)
	v_cmp_ge_f32_e64 s[66:67], v178, v140
	v_cmp_ge_f32_e64 s[50:51], v178, v139
	v_cmp_ge_f32_e32 vcc, v179, v140
	v_cmp_ge_f32_e64 s[52:53], v179, v139
	v_cndmask_b32_e64 v224, 0, 1, s[66:67]
	v_cndmask_b32_e64 v225, 0, 2, vcc
	s_andn2_b64 s[50:51], s[50:51], s[66:67]
	s_andn2_b64 s[52:53], s[52:53], vcc
	v_or_b32_e32 v228, v224, v225
	v_cmp_ge_f32_e64 s[66:67], v180, v140
	v_cmp_ge_f32_e64 s[54:55], v180, v139
	v_cmp_ge_f32_e32 vcc, v181, v140
	v_cmp_ge_f32_e64 s[56:57], v181, v139
	v_cndmask_b32_e64 v224, 0, 4, s[66:67]
	v_cndmask_b32_e64 v225, 0, 8, vcc
	s_andn2_b64 s[54:55], s[54:55], s[66:67]
	s_andn2_b64 s[56:57], s[56:57], vcc
	v_or3_b32 v228, v228, v224, v225
	v_cmp_ge_f32_e64 s[66:67], v182, v140
	v_cmp_ge_f32_e64 s[58:59], v182, v139
	v_cmp_ge_f32_e32 vcc, v183, v140
	v_cmp_ge_f32_e64 s[60:61], v183, v139
	v_cndmask_b32_e64 v224, 0, v201, s[66:67]
	v_cndmask_b32_e64 v225, 0, v200, vcc
	s_andn2_b64 s[58:59], s[58:59], s[66:67]
	s_andn2_b64 s[60:61], s[60:61], vcc
	v_or3_b32 v228, v228, v224, v225
	v_cmp_ge_f32_e64 s[66:67], v184, v140
	v_cmp_ge_f32_e64 s[62:63], v184, v139
	v_cmp_ge_f32_e32 vcc, v185, v140
	v_cmp_ge_f32_e64 s[64:65], v185, v139
	v_cndmask_b32_e64 v224, 0, v199, s[66:67]
	v_cndmask_b32_e64 v225, 0, v198, vcc
	s_andn2_b64 s[62:63], s[62:63], s[66:67]
	s_andn2_b64 s[64:65], s[64:65], vcc
	v_or3_b32 v228, v228, v224, v225
	v_lshlrev_b32_e32 v104, v143, v228
	ds_bpermute_b32 v105, v144, v104
	v_mov_b32_e32 v227, s96
	s_mov_b64 s[14:15], exec
	s_mov_b64 exec, s[50:51]
	ds_add_rtn_u32 v214, v142, v193
	s_mov_b64 exec, s[52:53]
	ds_add_rtn_u32 v215, v142, v193
	s_mov_b64 exec, s[54:55]
	ds_add_rtn_u32 v216, v142, v193
	s_mov_b64 exec, s[56:57]
	ds_add_rtn_u32 v217, v142, v193
	s_mov_b64 exec, s[58:59]
	ds_add_rtn_u32 v218, v142, v193
	s_mov_b64 exec, s[60:61]
	ds_add_rtn_u32 v219, v142, v193
	s_mov_b64 exec, s[62:63]
	ds_add_rtn_u32 v220, v142, v193
	s_mov_b64 exec, s[64:65]
	ds_add_rtn_u32 v221, v142, v193
	s_mov_b64 exec, s[50:51]
	v_xor_b32_e32 v206, v244, v178
	v_bfe_u32 v222, v206, 11, 10
	v_bfe_u32 v223, v206, 10, 1
	v_lshl_add_u32 v222, v222, 2, v128
	v_mad_u32_u24 v223, v223, v235, 1
	ds_add_u32 v222, v223
	s_mov_b64 exec, s[52:53]
	v_xor_b32_e32 v207, v244, v179
	v_bfe_u32 v222, v207, 11, 10
	v_bfe_u32 v223, v207, 10, 1
	v_lshl_add_u32 v222, v222, 2, v128
	v_mad_u32_u24 v223, v223, v235, 1
	ds_add_u32 v222, v223
	s_mov_b64 exec, s[54:55]
	v_xor_b32_e32 v208, v244, v180
	v_bfe_u32 v222, v208, 11, 10
	v_bfe_u32 v223, v208, 10, 1
	v_lshl_add_u32 v222, v222, 2, v128
	v_mad_u32_u24 v223, v223, v235, 1
	ds_add_u32 v222, v223
	s_mov_b64 exec, s[56:57]
	v_xor_b32_e32 v209, v244, v181
	v_bfe_u32 v222, v209, 11, 10
	v_bfe_u32 v223, v209, 10, 1
	v_lshl_add_u32 v222, v222, 2, v128
	v_mad_u32_u24 v223, v223, v235, 1
	ds_add_u32 v222, v223
	s_waitcnt lgkmcnt(8)
	s_mov_b64 exec, s[58:59]
	v_xor_b32_e32 v210, v244, v182
	v_bfe_u32 v222, v210, 11, 10
	v_bfe_u32 v223, v210, 10, 1
	v_lshl_add_u32 v222, v222, 2, v128
	v_mad_u32_u24 v223, v223, v235, 1
	ds_add_u32 v222, v223
	s_mov_b64 exec, s[60:61]
	v_xor_b32_e32 v211, v244, v183
	v_bfe_u32 v222, v211, 11, 10
	v_bfe_u32 v223, v211, 10, 1
	v_lshl_add_u32 v222, v222, 2, v128
	v_mad_u32_u24 v223, v223, v235, 1
	ds_add_u32 v222, v223
	s_mov_b64 exec, s[62:63]
	v_xor_b32_e32 v212, v244, v184
	v_bfe_u32 v222, v212, 11, 10
	v_bfe_u32 v223, v212, 10, 1
	v_lshl_add_u32 v222, v222, 2, v128
	v_mad_u32_u24 v223, v223, v235, 1
	ds_add_u32 v222, v223
	s_mov_b64 exec, s[64:65]
	v_xor_b32_e32 v213, v244, v185
	v_bfe_u32 v222, v213, 11, 10
	v_bfe_u32 v223, v213, 10, 1
	v_lshl_add_u32 v222, v222, 2, v128
	v_mad_u32_u24 v223, v223, v235, 1
	ds_add_u32 v222, v223
	s_waitcnt lgkmcnt(8)
	s_mov_b64 exec, s[14:15]
	v_or_b32_e32 v104, v105, v104
	ds_bpermute_b32 v105, v145, v104
	s_mov_b64 exec, s[50:51]
	v_cmp_lt_u32_e64 s[66:67], s0, v214
	s_add_i32 s85, s74, 0x0
	v_bfe_u32 v224, v206, 10, 11
	v_lshl_add_u32 v222, v214, 2, v141
	v_add3_u32 v224, v224, v124, s85
	s_andn2_b64 exec, exec, s[66:67]
	ds_write_b32 v222, v224
	s_mov_b64 exec, s[66:67]
	ds_write_b32 v227, v193
	s_mov_b64 exec, s[52:53]
	v_cmp_lt_u32_e64 s[66:67], s0, v215
	s_add_i32 s85, s74, 0x800
	v_bfe_u32 v224, v207, 10, 11
	v_lshl_add_u32 v222, v215, 2, v141
	v_add3_u32 v224, v224, v124, s85
	s_andn2_b64 exec, exec, s[66:67]
	ds_write_b32 v222, v224
	s_mov_b64 exec, s[66:67]
	ds_write_b32 v227, v193
	s_waitcnt lgkmcnt(8)
	s_mov_b64 exec, s[54:55]
	v_cmp_lt_u32_e64 s[66:67], s0, v216
	s_add_i32 s85, s74, 0x1000
	v_bfe_u32 v224, v208, 10, 11
	v_lshl_add_u32 v222, v216, 2, v141
	v_add3_u32 v224, v224, v124, s85
	s_andn2_b64 exec, exec, s[66:67]
	ds_write_b32 v222, v224
	s_mov_b64 exec, s[66:67]
	ds_write_b32 v227, v193
	s_mov_b64 exec, s[56:57]
	v_cmp_lt_u32_e64 s[66:67], s0, v217
	s_add_i32 s85, s74, 0x1800
	v_bfe_u32 v224, v209, 10, 11
	v_lshl_add_u32 v222, v217, 2, v141
	v_add3_u32 v224, v224, v124, s85
	s_andn2_b64 exec, exec, s[66:67]
	ds_write_b32 v222, v224
	s_mov_b64 exec, s[66:67]
	ds_write_b32 v227, v193
	s_waitcnt lgkmcnt(8)
	s_mov_b64 exec, s[58:59]
	v_cmp_lt_u32_e64 s[66:67], s0, v218
	s_add_i32 s85, s74, 0x8000
	v_bfe_u32 v224, v210, 10, 11
	v_lshl_add_u32 v222, v218, 2, v141
	v_add3_u32 v224, v224, v124, s85
	s_andn2_b64 exec, exec, s[66:67]
	ds_write_b32 v222, v224
	s_mov_b64 exec, s[66:67]
	ds_write_b32 v227, v193
	s_mov_b64 exec, s[60:61]
	v_cmp_lt_u32_e64 s[66:67], s0, v219
	s_add_i32 s85, s74, 0x8800
	v_bfe_u32 v224, v211, 10, 11
	v_lshl_add_u32 v222, v219, 2, v141
	v_add3_u32 v224, v224, v124, s85
	s_andn2_b64 exec, exec, s[66:67]
	ds_write_b32 v222, v224
	s_mov_b64 exec, s[66:67]
	ds_write_b32 v227, v193
	s_waitcnt lgkmcnt(8)
	s_mov_b64 exec, s[62:63]
	v_cmp_lt_u32_e64 s[66:67], s0, v220
	s_add_i32 s85, s74, 0x9000
	v_bfe_u32 v224, v212, 10, 11
	v_lshl_add_u32 v222, v220, 2, v141
	v_add3_u32 v224, v224, v124, s85
	s_andn2_b64 exec, exec, s[66:67]
	ds_write_b32 v222, v224
	s_mov_b64 exec, s[66:67]
	ds_write_b32 v227, v193
	s_mov_b64 exec, s[64:65]
	v_cmp_lt_u32_e64 s[66:67], s0, v221
	s_add_i32 s85, s74, 0x9800
	v_bfe_u32 v224, v213, 10, 11
	v_lshl_add_u32 v222, v221, 2, v141
	v_add3_u32 v224, v224, v124, s85
	s_andn2_b64 exec, exec, s[66:67]
	ds_write_b32 v222, v224
	s_mov_b64 exec, s[66:67]
	ds_write_b32 v227, v193
	s_mov_b64 exec, s[14:15]
	s_and_saveexec_b64 s[14:15], s[38:39]
	v_or_b32_e32 v106, v104, v105
	v_lshl_add_u64 v[104:105], v[122:123], 0, s[74:75]
	v_add_co_u32_e32 v104, vcc, 0x3f700000, v104
	s_nop 1
	v_addc_co_u32_e32 v105, vcc, 0, v105, vcc
	global_store_dword v[104:105], v106, off
	s_or_b64 exec, exec, s[14:15]
	s_add_u32 s74, s74, 0x80000
	s_addc_u32 s75, s75, 0
	s_add_i32 s31, s31, 8
	s_cmp_ge_i32 s31, s32
	s_cbranch_scc1 .Lpb2_done
.Lpb2_i2:
	s_add_i32 s85, s31, 16
	s_min_i32 s85, s85, 0xff
	v_lshl_add_u32 v233, s85, 11, v230
	global_load_dwordx4 v[178:181], v233, s[100:101]
	global_load_dwordx4 v[182:185], v233, s[100:101] offset:1024
	s_waitcnt vmcnt(6)
	v_cmp_ge_f32_e64 s[66:67], v236, v140
	v_cmp_ge_f32_e64 s[50:51], v236, v139
	v_cmp_ge_f32_e32 vcc, v237, v140
	v_cmp_ge_f32_e64 s[52:53], v237, v139
	v_cndmask_b32_e64 v224, 0, 1, s[66:67]
	v_cndmask_b32_e64 v225, 0, 2, vcc
	s_andn2_b64 s[50:51], s[50:51], s[66:67]
	s_andn2_b64 s[52:53], s[52:53], vcc
	v_or_b32_e32 v228, v224, v225
	v_cmp_ge_f32_e64 s[66:67], v238, v140
	v_cmp_ge_f32_e64 s[54:55], v238, v139
	v_cmp_ge_f32_e32 vcc, v239, v140
	v_cmp_ge_f32_e64 s[56:57], v239, v139
	v_cndmask_b32_e64 v224, 0, 4, s[66:67]
	v_cndmask_b32_e64 v225, 0, 8, vcc
	s_andn2_b64 s[54:55], s[54:55], s[66:67]
	s_andn2_b64 s[56:57], s[56:57], vcc
	v_or3_b32 v228, v228, v224, v225
	v_cmp_ge_f32_e64 s[66:67], v240, v140
	v_cmp_ge_f32_e64 s[58:59], v240, v139
	v_cmp_ge_f32_e32 vcc, v241, v140
	v_cmp_ge_f32_e64 s[60:61], v241, v139
	v_cndmask_b32_e64 v224, 0, v201, s[66:67]
	v_cndmask_b32_e64 v225, 0, v200, vcc
	s_andn2_b64 s[58:59], s[58:59], s[66:67]
	s_andn2_b64 s[60:61], s[60:61], vcc
	v_or3_b32 v228, v228, v224, v225
	v_cmp_ge_f32_e64 s[66:67], v242, v140
	v_cmp_ge_f32_e64 s[62:63], v242, v139
	v_cmp_ge_f32_e32 vcc, v243, v140
	v_cmp_ge_f32_e64 s[64:65], v243, v139
	v_cndmask_b32_e64 v224, 0, v199, s[66:67]
	v_cndmask_b32_e64 v225, 0, v198, vcc
	s_andn2_b64 s[62:63], s[62:63], s[66:67]
	s_andn2_b64 s[64:65], s[64:65], vcc
	v_or3_b32 v228, v228, v224, v225
	v_lshlrev_b32_e32 v104, v143, v228
	ds_bpermute_b32 v105, v144, v104
	v_mov_b32_e32 v227, s96
	s_mov_b64 s[14:15], exec
	s_mov_b64 exec, s[50:51]
	ds_add_rtn_u32 v214, v142, v193
	s_mov_b64 exec, s[52:53]
	ds_add_rtn_u32 v215, v142, v193
	s_mov_b64 exec, s[54:55]
	ds_add_rtn_u32 v216, v142, v193
	s_mov_b64 exec, s[56:57]
	ds_add_rtn_u32 v217, v142, v193
	s_mov_b64 exec, s[58:59]
	ds_add_rtn_u32 v218, v142, v193
	s_mov_b64 exec, s[60:61]
	ds_add_rtn_u32 v219, v142, v193
	s_mov_b64 exec, s[62:63]
	ds_add_rtn_u32 v220, v142, v193
	s_mov_b64 exec, s[64:65]
	ds_add_rtn_u32 v221, v142, v193
	s_mov_b64 exec, s[50:51]
	v_xor_b32_e32 v206, v244, v236
	v_bfe_u32 v222, v206, 11, 10
	v_bfe_u32 v223, v206, 10, 1
	v_lshl_add_u32 v222, v222, 2, v128
	v_mad_u32_u24 v223, v223, v235, 1
	ds_add_u32 v222, v223
	s_mov_b64 exec, s[52:53]
	v_xor_b32_e32 v207, v244, v237
	v_bfe_u32 v222, v207, 11, 10
	v_bfe_u32 v223, v207, 10, 1
	v_lshl_add_u32 v222, v222, 2, v128
	v_mad_u32_u24 v223, v223, v235, 1
	ds_add_u32 v222, v223
	s_mov_b64 exec, s[54:55]
	v_xor_b32_e32 v208, v244, v238
	v_bfe_u32 v222, v208, 11, 10
	v_bfe_u32 v223, v208, 10, 1
	v_lshl_add_u32 v222, v222, 2, v128
	v_mad_u32_u24 v223, v223, v235, 1
	ds_add_u32 v222, v223
	s_mov_b64 exec, s[56:57]
	v_xor_b32_e32 v209, v244, v239
	v_bfe_u32 v222, v209, 11, 10
	v_bfe_u32 v223, v209, 10, 1
	v_lshl_add_u32 v222, v222, 2, v128
	v_mad_u32_u24 v223, v223, v235, 1
	ds_add_u32 v222, v223
	s_waitcnt lgkmcnt(8)
	s_mov_b64 exec, s[58:59]
	v_xor_b32_e32 v210, v244, v240
	v_bfe_u32 v222, v210, 11, 10
	v_bfe_u32 v223, v210, 10, 1
	v_lshl_add_u32 v222, v222, 2, v128
	v_mad_u32_u24 v223, v223, v235, 1
	ds_add_u32 v222, v223
	s_mov_b64 exec, s[60:61]
	v_xor_b32_e32 v211, v244, v241
	v_bfe_u32 v222, v211, 11, 10
	v_bfe_u32 v223, v211, 10, 1
	v_lshl_add_u32 v222, v222, 2, v128
	v_mad_u32_u24 v223, v223, v235, 1
	ds_add_u32 v222, v223
	s_mov_b64 exec, s[62:63]
	v_xor_b32_e32 v212, v244, v242
	v_bfe_u32 v222, v212, 11, 10
	v_bfe_u32 v223, v212, 10, 1
	v_lshl_add_u32 v222, v222, 2, v128
	v_mad_u32_u24 v223, v223, v235, 1
	ds_add_u32 v222, v223
	s_mov_b64 exec, s[64:65]
	v_xor_b32_e32 v213, v244, v243
	v_bfe_u32 v222, v213, 11, 10
	v_bfe_u32 v223, v213, 10, 1
	v_lshl_add_u32 v222, v222, 2, v128
	v_mad_u32_u24 v223, v223, v235, 1
	ds_add_u32 v222, v223
	s_waitcnt lgkmcnt(8)
	s_mov_b64 exec, s[14:15]
	v_or_b32_e32 v104, v105, v104
	ds_bpermute_b32 v105, v145, v104
	s_mov_b64 exec, s[50:51]
	v_cmp_lt_u32_e64 s[66:67], s0, v214
	s_add_i32 s85, s74, 0x0
	v_bfe_u32 v224, v206, 10, 11
	v_lshl_add_u32 v222, v214, 2, v141
	v_add3_u32 v224, v224, v124, s85
	s_andn2_b64 exec, exec, s[66:67]
	ds_write_b32 v222, v224
	s_mov_b64 exec, s[66:67]
	ds_write_b32 v227, v193
	s_mov_b64 exec, s[52:53]
	v_cmp_lt_u32_e64 s[66:67], s0, v215
	s_add_i32 s85, s74, 0x800
	v_bfe_u32 v224, v207, 10, 11
	v_lshl_add_u32 v222, v215, 2, v141
	v_add3_u32 v224, v224, v124, s85
	s_andn2_b64 exec, exec, s[66:67]
	ds_write_b32 v222, v224
	s_mov_b64 exec, s[66:67]
	ds_write_b32 v227, v193
	s_waitcnt lgkmcnt(8)
	s_mov_b64 exec, s[54:55]
	v_cmp_lt_u32_e64 s[66:67], s0, v216
	s_add_i32 s85, s74, 0x1000
	v_bfe_u32 v224, v208, 10, 11
	v_lshl_add_u32 v222, v216, 2, v141
	v_add3_u32 v224, v224, v124, s85
	s_andn2_b64 exec, exec, s[66:67]
	ds_write_b32 v222, v224
	s_mov_b64 exec, s[66:67]
	ds_write_b32 v227, v193
	s_mov_b64 exec, s[56:57]
	v_cmp_lt_u32_e64 s[66:67], s0, v217
	s_add_i32 s85, s74, 0x1800
	v_bfe_u32 v224, v209, 10, 11
	v_lshl_add_u32 v222, v217, 2, v141
	v_add3_u32 v224, v224, v124, s85
	s_andn2_b64 exec, exec, s[66:67]
	ds_write_b32 v222, v224
	s_mov_b64 exec, s[66:67]
	ds_write_b32 v227, v193
	s_waitcnt lgkmcnt(8)
	s_mov_b64 exec, s[58:59]
	v_cmp_lt_u32_e64 s[66:67], s0, v218
	s_add_i32 s85, s74, 0x8000
	v_bfe_u32 v224, v210, 10, 11
	v_lshl_add_u32 v222, v218, 2, v141
	v_add3_u32 v224, v224, v124, s85
	s_andn2_b64 exec, exec, s[66:67]
	ds_write_b32 v222, v224
	s_mov_b64 exec, s[66:67]
	ds_write_b32 v227, v193
	s_mov_b64 exec, s[60:61]
	v_cmp_lt_u32_e64 s[66:67], s0, v219
	s_add_i32 s85, s74, 0x8800
	v_bfe_u32 v224, v211, 10, 11
	v_lshl_add_u32 v222, v219, 2, v141
	v_add3_u32 v224, v224, v124, s85
	s_andn2_b64 exec, exec, s[66:67]
	ds_write_b32 v222, v224
	s_mov_b64 exec, s[66:67]
	ds_write_b32 v227, v193
	s_waitcnt lgkmcnt(8)
	s_mov_b64 exec, s[62:63]
	v_cmp_lt_u32_e64 s[66:67], s0, v220
	s_add_i32 s85, s74, 0x9000
	v_bfe_u32 v224, v212, 10, 11
	v_lshl_add_u32 v222, v220, 2, v141
	v_add3_u32 v224, v224, v124, s85
	s_andn2_b64 exec, exec, s[66:67]
	ds_write_b32 v222, v224
	s_mov_b64 exec, s[66:67]
	ds_write_b32 v227, v193
	s_mov_b64 exec, s[64:65]
	v_cmp_lt_u32_e64 s[66:67], s0, v221
	s_add_i32 s85, s74, 0x9800
	v_bfe_u32 v224, v213, 10, 11
	v_lshl_add_u32 v222, v221, 2, v141
	v_add3_u32 v224, v224, v124, s85
	s_andn2_b64 exec, exec, s[66:67]
	ds_write_b32 v222, v224
	s_mov_b64 exec, s[66:67]
	ds_write_b32 v227, v193
	s_mov_b64 exec, s[14:15]
	s_and_saveexec_b64 s[14:15], s[38:39]
	v_or_b32_e32 v106, v104, v105
	v_lshl_add_u64 v[104:105], v[122:123], 0, s[74:75]
	v_add_co_u32_e32 v104, vcc, 0x3f700000, v104
	s_nop 1
	v_addc_co_u32_e32 v105, vcc, 0, v105, vcc
	global_store_dword v[104:105], v106, off
	s_or_b64 exec, exec, s[14:15]
	s_add_u32 s74, s74, 0x80000
	s_addc_u32 s75, s75, 0
	s_add_i32 s31, s31, 8
	s_cmp_ge_i32 s31, s32
	s_cbranch_scc0 .Lpb2_i0
